# LN1 router: no drain of the wave's own pass-1 stores before the first operand loads (the first counted wait covers them)
# speedup vs baseline: 1.0099x; 1.0010x over previous
.LBB0_3237:
	s_add_i32 s10, s8, s9
	s_and_b32 s10, s10, 15
	s_lshl_b32 s64, s10, 6
	v_lshl_add_u64 v[76:77], v[32:33], 0, s[64:65]
	v_lshl_add_u64 v[78:79], v[34:35], 0, s[64:65]
	s_mul_i32 s64, s10, 0xc00
	v_lshl_add_u64 v[80:81], v[36:37], 0, s[64:65]
	global_load_dwordx4 v[56:59], v[76:77], off
	global_load_dwordx4 v[60:63], v[78:79], off
	global_load_dwordx4 v[88:91], v[80:81], off
	global_load_dwordx4 v[92:95], v[80:81], off offset:1024
	global_load_dwordx4 v[96:99], v[80:81], off offset:2048
